# baseline (speedup 1.0000x reference)
.LBB8_12:
	ds_read_b128 v[146:149], v188
	ds_read_b128 v[150:153], v188 offset:1024
	ds_read_b128 v[154:157], v188 offset:2048
	ds_read_b128 v[158:161], v188 offset:3072
	ds_read_b128 v[226:229], v190
	ds_read_b128 v[230:233], v190 offset:1024
	ds_read_b128 v[234:237], v190 offset:2048
	ds_read_b128 v[238:241], v190 offset:3072
	s_cmp_eq_u32 s51, s61
	s_cselect_b64 s[66:67], -1, 0
	s_add_i32 s61, s61, 2
	s_and_b64 s[34:35], s[66:67], exec
	s_cselect_b32 s35, s31, s60
	s_cselect_b32 s34, s30, s59
	s_cselect_b32 s64, s37, s57
	s_lshl_b32 s65, s64, 13
	s_and_b64 s[66:67], s[66:67], exec
	s_cselect_b32 s63, 0, s62
	s_add_i32 s68, s65, s63
	ds_read_b128 v[194:197], v189
	ds_read_b128 v[198:201], v189 offset:1024
	ds_read_b128 v[202:205], v189 offset:2048
	ds_read_b128 v[206:209], v189 offset:3072
	ds_read_b128 v[210:213], v189 offset:4096
	ds_read_b128 v[214:217], v189 offset:5120
	ds_read_b128 v[218:221], v189 offset:6144
	ds_read_b128 v[222:225], v189 offset:7168
	s_ashr_i32 s69, s68, 31
	s_waitcnt vmcnt(0)
	s_lshl_b64 s[66:67], s[68:69], 1
	v_pk_add_f16 v14, v14, v10
	v_pk_add_f16 v15, v15, v11
	v_pk_add_f16 v16, v16, v12
	v_pk_add_f16 v17, v17, v13
	s_add_u32 s70, s8, s66
	v_pk_max_f16 v17, v17, 0
	v_pk_max_f16 v16, v16, 0
	v_pk_max_f16 v15, v15, 0
	v_pk_max_f16 v14, v14, 0
	v_pk_add_f16 v6, v6, v10
	v_pk_add_f16 v7, v7, v11
	v_pk_add_f16 v8, v8, v12
	v_pk_add_f16 v9, v9, v13
	s_addc_u32 s71, s9, s67
	s_add_i32 s68, s68, s65
	v_pk_max_f16 v9, v9, 0
	v_pk_max_f16 v8, v8, 0
	v_pk_max_f16 v7, v7, 0
	v_pk_max_f16 v6, v6, 0
	ds_write_b128 v186, v[14:17] offset:49152
	ds_write_b128 v186, v[6:9] offset:57344
	s_ashr_i32 s69, s68, 31
	s_lshl_b32 s66, s64, 14
	s_lshl_b64 s[68:69], s[68:69], 1
	s_nop 4
	global_load_dwordx4 v[6:9], v184, s[70:71]
	s_add_u32 s68, s10, s68
	global_load_dwordx4 v[10:13], v185, s[70:71]
	s_addc_u32 s69, s11, s69
	global_load_dwordx4 v[14:17], v183, s[68:69]
	s_waitcnt lgkmcnt(2)
	s_barrier
	s_waitcnt lgkmcnt(0)
	s_setprio 1
	s_waitcnt lgkmcnt(0)
	v_mfma_f32_16x16x32_f16 v[138:141], v[146:149], v[194:197], v[138:141]
	v_mfma_f32_16x16x32_f16 v[142:145], v[154:157], v[194:197], v[142:145]
	v_mfma_f32_16x16x32_f16 v[126:129], v[146:149], v[202:205], v[126:129]
	v_mfma_f32_16x16x32_f16 v[122:125], v[154:157], v[202:205], v[122:125]
	v_mfma_f32_16x16x32_f16 v[110:113], v[146:149], v[210:213], v[110:113]
	v_mfma_f32_16x16x32_f16 v[106:109], v[154:157], v[210:213], v[106:109]
	v_mfma_f32_16x16x32_f16 v[94:97], v[146:149], v[218:221], v[94:97]
	v_mfma_f32_16x16x32_f16 v[90:93], v[154:157], v[218:221], v[90:93]
	v_mfma_f32_16x16x32_f16 v[138:141], v[150:153], v[198:201], v[138:141]
	v_mfma_f32_16x16x32_f16 v[142:145], v[158:161], v[198:201], v[142:145]
	v_mfma_f32_16x16x32_f16 v[126:129], v[150:153], v[206:209], v[126:129]
	v_mfma_f32_16x16x32_f16 v[122:125], v[158:161], v[206:209], v[122:125]
	v_mfma_f32_16x16x32_f16 v[110:113], v[150:153], v[214:217], v[110:113]
	v_mfma_f32_16x16x32_f16 v[106:109], v[158:161], v[214:217], v[106:109]
	v_mfma_f32_16x16x32_f16 v[94:97], v[150:153], v[222:225], v[94:97]
	v_mfma_f32_16x16x32_f16 v[90:93], v[158:161], v[222:225], v[90:93]
	s_setprio 0
	s_waitcnt lgkmcnt(0)
	s_setprio 1
	s_waitcnt lgkmcnt(0)
	v_mfma_f32_16x16x32_f16 v[134:137], v[226:229], v[194:197], v[134:137]
	v_mfma_f32_16x16x32_f16 v[130:133], v[234:237], v[194:197], v[130:133]
	v_mfma_f32_16x16x32_f16 v[118:121], v[226:229], v[202:205], v[118:121]
	v_mfma_f32_16x16x32_f16 v[114:117], v[234:237], v[202:205], v[114:117]
	v_mfma_f32_16x16x32_f16 v[102:105], v[226:229], v[210:213], v[102:105]
	v_mfma_f32_16x16x32_f16 v[98:101], v[234:237], v[210:213], v[98:101]
	v_mfma_f32_16x16x32_f16 v[86:89], v[226:229], v[218:221], v[86:89]
	v_mfma_f32_16x16x32_f16 v[82:85], v[234:237], v[218:221], v[82:85]
	ds_read_b128 v[194:197], v189 offset:16384
	ds_read_b128 v[202:205], v189 offset:18432
	ds_read_b128 v[210:213], v189 offset:20480
	ds_read_b128 v[218:221], v189 offset:22528
	v_mfma_f32_16x16x32_f16 v[134:137], v[230:233], v[198:201], v[134:137]
	v_mfma_f32_16x16x32_f16 v[130:133], v[238:241], v[198:201], v[130:133]
	v_mfma_f32_16x16x32_f16 v[118:121], v[230:233], v[206:209], v[118:121]
	v_mfma_f32_16x16x32_f16 v[114:117], v[238:241], v[206:209], v[114:117]
	v_mfma_f32_16x16x32_f16 v[102:105], v[230:233], v[214:217], v[102:105]
	v_mfma_f32_16x16x32_f16 v[98:101], v[238:241], v[214:217], v[98:101]
	v_mfma_f32_16x16x32_f16 v[86:89], v[230:233], v[222:225], v[86:89]
	v_mfma_f32_16x16x32_f16 v[82:85], v[238:241], v[222:225], v[82:85]
	ds_read_b128 v[198:201], v189 offset:17408
	ds_read_b128 v[206:209], v189 offset:19456
	ds_read_b128 v[214:217], v189 offset:21504
	ds_read_b128 v[222:225], v189 offset:23552
	s_waitcnt lgkmcnt(4)
	s_setprio 1
	s_waitcnt lgkmcnt(4)
	v_mfma_f32_16x16x32_f16 v[78:81], v[146:149], v[194:197], v[78:81]
	v_mfma_f32_16x16x32_f16 v[74:77], v[154:157], v[194:197], v[74:77]
	v_mfma_f32_16x16x32_f16 v[62:65], v[146:149], v[202:205], v[62:65]
	v_mfma_f32_16x16x32_f16 v[58:61], v[154:157], v[202:205], v[58:61]
	v_mfma_f32_16x16x32_f16 v[46:49], v[146:149], v[210:213], v[46:49]
	v_mfma_f32_16x16x32_f16 v[42:45], v[154:157], v[210:213], v[42:45]
	v_mfma_f32_16x16x32_f16 v[30:33], v[146:149], v[218:221], v[30:33]
	v_mfma_f32_16x16x32_f16 v[26:29], v[154:157], v[218:221], v[26:29]
	s_waitcnt lgkmcnt(0)
	v_mfma_f32_16x16x32_f16 v[78:81], v[150:153], v[198:201], v[78:81]
	v_mfma_f32_16x16x32_f16 v[74:77], v[158:161], v[198:201], v[74:77]
	v_mfma_f32_16x16x32_f16 v[62:65], v[150:153], v[206:209], v[62:65]
	v_mfma_f32_16x16x32_f16 v[58:61], v[158:161], v[206:209], v[58:61]
	v_mfma_f32_16x16x32_f16 v[46:49], v[150:153], v[214:217], v[46:49]
	v_mfma_f32_16x16x32_f16 v[42:45], v[158:161], v[214:217], v[42:45]
	v_mfma_f32_16x16x32_f16 v[30:33], v[150:153], v[222:225], v[30:33]
	v_mfma_f32_16x16x32_f16 v[26:29], v[158:161], v[222:225], v[26:29]
	s_setprio 0
	s_setprio 1
	v_mfma_f32_16x16x32_f16 v[70:73], v[226:229], v[194:197], v[70:73]
	v_mfma_f32_16x16x32_f16 v[66:69], v[234:237], v[194:197], v[66:69]
	v_mfma_f32_16x16x32_f16 v[54:57], v[226:229], v[202:205], v[54:57]
	v_mfma_f32_16x16x32_f16 v[50:53], v[234:237], v[202:205], v[50:53]
	v_mfma_f32_16x16x32_f16 v[38:41], v[226:229], v[210:213], v[38:41]
	v_mfma_f32_16x16x32_f16 v[34:37], v[234:237], v[210:213], v[34:37]
	v_mfma_f32_16x16x32_f16 v[22:25], v[226:229], v[218:221], v[22:25]
	v_mfma_f32_16x16x32_f16 v[18:21], v[234:237], v[218:221], v[18:21]
	v_mfma_f32_16x16x32_f16 v[70:73], v[230:233], v[198:201], v[70:73]
	v_mfma_f32_16x16x32_f16 v[66:69], v[238:241], v[198:201], v[66:69]
	v_mfma_f32_16x16x32_f16 v[54:57], v[230:233], v[206:209], v[54:57]
	v_mfma_f32_16x16x32_f16 v[50:53], v[238:241], v[206:209], v[50:53]
	v_mfma_f32_16x16x32_f16 v[38:41], v[230:233], v[214:217], v[38:41]
	v_mfma_f32_16x16x32_f16 v[34:37], v[238:241], v[214:217], v[34:37]
	v_mfma_f32_16x16x32_f16 v[22:25], v[230:233], v[222:225], v[22:25]
	v_mfma_f32_16x16x32_f16 v[18:21], v[238:241], v[222:225], v[18:21]
	s_setprio 0
	s_or_b32 s64, s65, 0x1000
	s_add_i32 s68, s64, s63
	s_barrier
	s_add_i32 s81, s53, s45
	v_lshl_add_u64 v[170:171], s[34:35], 0, v[162:163]
	s_mov_b32 m0, s81
	global_load_lds_dwordx4 v[170:171], off
	v_lshl_add_u64 v[242:243], s[34:35], 0, v[164:165]
	s_add_i32 m0, s81, 0x2000
	s_nop 0
	global_load_lds_dwordx4 v[242:243], off
	s_add_u32 s34, s34, s22
	s_addc_u32 s35, s35, s23
	s_add_i32 s82, s54, s45
	v_lshl_add_u64 v[244:245], s[34:35], 0, v[162:163]
	s_mov_b32 m0, s82
	v_lshl_add_u64 v[246:247], s[34:35], 0, v[164:165]
	global_load_lds_dwordx4 v[244:245], off
	s_add_i32 m0, s82, 0x2000
	s_nop 0
	global_load_lds_dwordx4 v[246:247], off
	s_ashr_i32 s69, s68, 31
	s_lshl_b64 s[68:69], s[68:69], 1
	s_waitcnt vmcnt(4)
	s_add_u32 s68, s8, s68
	v_pk_add_f16 v6, v6, v14
	v_pk_add_f16 v7, v7, v15
	v_pk_add_f16 v8, v8, v16
	v_pk_add_f16 v9, v9, v17
	s_addc_u32 s69, s9, s69
	s_or_b32 s67, s66, 0x2000
	v_pk_max_f16 v9, v9, 0
	v_pk_max_f16 v8, v8, 0
	v_pk_max_f16 v7, v7, 0
	v_pk_max_f16 v6, v6, 0
	v_pk_add_f16 v10, v10, v14
	v_pk_add_f16 v11, v11, v15
	v_pk_add_f16 v12, v12, v16
	v_pk_add_f16 v13, v13, v17
	s_add_i32 s70, s67, s63
	v_pk_max_f16 v13, v13, 0
	v_pk_max_f16 v12, v12, 0
	v_pk_max_f16 v11, v11, 0
	v_pk_max_f16 v10, v10, 0
	ds_write_b128 v186, v[6:9]
	ds_write_b128 v186, v[10:13] offset:8192
	s_ashr_i32 s71, s70, 31
	s_lshl_b64 s[70:71], s[70:71], 1
	s_nop 4
	global_load_dwordx4 v[6:9], v184, s[68:69]
	s_add_u32 s70, s10, s70
	global_load_dwordx4 v[10:13], v185, s[68:69]
	s_addc_u32 s71, s11, s71
	global_load_dwordx4 v[14:17], v183, s[70:71]
	s_waitcnt lgkmcnt(2)
	s_barrier
	ds_read_b128 v[146:149], v191
	ds_read_b128 v[150:153], v191 offset:1024
	ds_read_b128 v[154:157], v191 offset:2048
	ds_read_b128 v[158:161], v191 offset:3072
	ds_read_b128 v[226:229], v192
	ds_read_b128 v[230:233], v192 offset:1024
	ds_read_b128 v[234:237], v192 offset:2048
	ds_read_b128 v[238:241], v192 offset:3072
	s_or_b32 s70, s63, 64
	s_ashr_i32 s35, s65, 31
	s_ashr_i32 s69, s63, 31
	s_add_u32 s34, s63, s65
	s_addc_u32 s35, s69, s35
	s_lshl_b64 s[34:35], s[34:35], 1
	s_add_u32 s34, s8, s34
	s_addc_u32 s35, s9, s35
	s_add_u32 s34, s34, 0x80
	ds_read_b128 v[194:197], v189 offset:32768
	ds_read_b128 v[198:201], v189 offset:33792
	ds_read_b128 v[202:205], v189 offset:34816
	ds_read_b128 v[206:209], v189 offset:35840
	ds_read_b128 v[210:213], v189 offset:36864
	ds_read_b128 v[214:217], v189 offset:37888
	ds_read_b128 v[218:221], v189 offset:38912
	ds_read_b128 v[222:225], v189 offset:39936
	s_addc_u32 s35, s35, 0
	s_ashr_i32 s65, s66, 31
	s_waitcnt vmcnt(0)
	s_add_u32 s68, s63, s66
	v_pk_add_f16 v6, v6, v14
	v_pk_add_f16 v7, v7, v15
	v_pk_add_f16 v8, v8, v16
	v_pk_add_f16 v9, v9, v17
	s_addc_u32 s69, s69, s65
	v_pk_max_f16 v9, v9, 0
	v_pk_max_f16 v8, v8, 0
	v_pk_max_f16 v7, v7, 0
	v_pk_max_f16 v6, v6, 0
	v_pk_add_f16 v10, v10, v14
	v_pk_add_f16 v11, v11, v15
	v_pk_add_f16 v12, v12, v16
	v_pk_add_f16 v13, v13, v17
	s_lshl_b64 s[68:69], s[68:69], 1
	v_pk_max_f16 v13, v13, 0
	v_pk_max_f16 v12, v12, 0
	v_pk_max_f16 v11, v11, 0
	v_pk_max_f16 v10, v10, 0
	ds_write_b128 v186, v[6:9] offset:16384
	ds_write_b128 v186, v[10:13] offset:24576
	s_add_u32 s63, s10, s68
	s_addc_u32 s65, s11, s69
	s_nop 4
	global_load_dwordx4 v[6:9], v184, s[34:35]
	s_add_u32 s68, s63, 0x80
	global_load_dwordx4 v[10:13], v185, s[34:35]
	s_addc_u32 s69, s65, 0
	global_load_dwordx4 v[14:17], v183, s[68:69]
	s_waitcnt lgkmcnt(2)
	s_barrier
	s_waitcnt lgkmcnt(0)
	s_setprio 1
	s_waitcnt lgkmcnt(0)
	v_mfma_f32_16x16x32_f16 v[138:141], v[146:149], v[194:197], v[138:141]
	v_mfma_f32_16x16x32_f16 v[142:145], v[154:157], v[194:197], v[142:145]
	v_mfma_f32_16x16x32_f16 v[126:129], v[146:149], v[202:205], v[126:129]
	v_mfma_f32_16x16x32_f16 v[122:125], v[154:157], v[202:205], v[122:125]
	v_mfma_f32_16x16x32_f16 v[110:113], v[146:149], v[210:213], v[110:113]
	v_mfma_f32_16x16x32_f16 v[106:109], v[154:157], v[210:213], v[106:109]
	v_mfma_f32_16x16x32_f16 v[94:97], v[146:149], v[218:221], v[94:97]
	v_mfma_f32_16x16x32_f16 v[90:93], v[154:157], v[218:221], v[90:93]
	v_mfma_f32_16x16x32_f16 v[138:141], v[150:153], v[198:201], v[138:141]
	v_mfma_f32_16x16x32_f16 v[142:145], v[158:161], v[198:201], v[142:145]
	v_mfma_f32_16x16x32_f16 v[126:129], v[150:153], v[206:209], v[126:129]
	v_mfma_f32_16x16x32_f16 v[122:125], v[158:161], v[206:209], v[122:125]
	v_mfma_f32_16x16x32_f16 v[110:113], v[150:153], v[214:217], v[110:113]
	v_mfma_f32_16x16x32_f16 v[106:109], v[158:161], v[214:217], v[106:109]
	v_mfma_f32_16x16x32_f16 v[94:97], v[150:153], v[222:225], v[94:97]
	v_mfma_f32_16x16x32_f16 v[90:93], v[158:161], v[222:225], v[90:93]
	s_setprio 0
	s_waitcnt lgkmcnt(0)
	s_setprio 1
	s_waitcnt lgkmcnt(0)
	v_mfma_f32_16x16x32_f16 v[134:137], v[226:229], v[194:197], v[134:137]
	v_mfma_f32_16x16x32_f16 v[130:133], v[234:237], v[194:197], v[130:133]
	v_mfma_f32_16x16x32_f16 v[118:121], v[226:229], v[202:205], v[118:121]
	v_mfma_f32_16x16x32_f16 v[114:117], v[234:237], v[202:205], v[114:117]
	v_mfma_f32_16x16x32_f16 v[102:105], v[226:229], v[210:213], v[102:105]
	v_mfma_f32_16x16x32_f16 v[98:101], v[234:237], v[210:213], v[98:101]
	v_mfma_f32_16x16x32_f16 v[86:89], v[226:229], v[218:221], v[86:89]
	v_mfma_f32_16x16x32_f16 v[82:85], v[234:237], v[218:221], v[82:85]
	ds_read_b128 v[194:197], v189 offset:49152
	ds_read_b128 v[202:205], v189 offset:51200
	ds_read_b128 v[210:213], v189 offset:53248
	ds_read_b128 v[218:221], v189 offset:55296
	v_mfma_f32_16x16x32_f16 v[134:137], v[230:233], v[198:201], v[134:137]
	v_mfma_f32_16x16x32_f16 v[130:133], v[238:241], v[198:201], v[130:133]
	v_mfma_f32_16x16x32_f16 v[118:121], v[230:233], v[206:209], v[118:121]
	v_mfma_f32_16x16x32_f16 v[114:117], v[238:241], v[206:209], v[114:117]
	v_mfma_f32_16x16x32_f16 v[102:105], v[230:233], v[214:217], v[102:105]
	v_mfma_f32_16x16x32_f16 v[98:101], v[238:241], v[214:217], v[98:101]
	v_mfma_f32_16x16x32_f16 v[86:89], v[230:233], v[222:225], v[86:89]
	v_mfma_f32_16x16x32_f16 v[82:85], v[238:241], v[222:225], v[82:85]
	ds_read_b128 v[198:201], v189 offset:50176
	ds_read_b128 v[206:209], v189 offset:52224
	ds_read_b128 v[214:217], v189 offset:54272
	ds_read_b128 v[222:225], v189 offset:56320
	s_waitcnt lgkmcnt(4)
	s_setprio 1
	s_waitcnt lgkmcnt(4)
	v_mfma_f32_16x16x32_f16 v[78:81], v[146:149], v[194:197], v[78:81]
	v_mfma_f32_16x16x32_f16 v[74:77], v[154:157], v[194:197], v[74:77]
	v_mfma_f32_16x16x32_f16 v[62:65], v[146:149], v[202:205], v[62:65]
	v_mfma_f32_16x16x32_f16 v[58:61], v[154:157], v[202:205], v[58:61]
	v_mfma_f32_16x16x32_f16 v[46:49], v[146:149], v[210:213], v[46:49]
	v_mfma_f32_16x16x32_f16 v[42:45], v[154:157], v[210:213], v[42:45]
	v_mfma_f32_16x16x32_f16 v[30:33], v[146:149], v[218:221], v[30:33]
	v_mfma_f32_16x16x32_f16 v[26:29], v[154:157], v[218:221], v[26:29]
	s_waitcnt lgkmcnt(0)
	v_mfma_f32_16x16x32_f16 v[78:81], v[150:153], v[198:201], v[78:81]
	v_mfma_f32_16x16x32_f16 v[74:77], v[158:161], v[198:201], v[74:77]
	v_mfma_f32_16x16x32_f16 v[62:65], v[150:153], v[206:209], v[62:65]
	v_mfma_f32_16x16x32_f16 v[58:61], v[158:161], v[206:209], v[58:61]
	v_mfma_f32_16x16x32_f16 v[46:49], v[150:153], v[214:217], v[46:49]
	v_mfma_f32_16x16x32_f16 v[42:45], v[158:161], v[214:217], v[42:45]
	v_mfma_f32_16x16x32_f16 v[30:33], v[150:153], v[222:225], v[30:33]
	v_mfma_f32_16x16x32_f16 v[26:29], v[158:161], v[222:225], v[26:29]
	s_setprio 0
	s_setprio 1
	v_mfma_f32_16x16x32_f16 v[70:73], v[226:229], v[194:197], v[70:73]
	v_mfma_f32_16x16x32_f16 v[66:69], v[234:237], v[194:197], v[66:69]
	v_mfma_f32_16x16x32_f16 v[54:57], v[226:229], v[202:205], v[54:57]
	v_mfma_f32_16x16x32_f16 v[50:53], v[234:237], v[202:205], v[50:53]
	v_mfma_f32_16x16x32_f16 v[38:41], v[226:229], v[210:213], v[38:41]
	v_mfma_f32_16x16x32_f16 v[34:37], v[234:237], v[210:213], v[34:37]
	v_mfma_f32_16x16x32_f16 v[22:25], v[226:229], v[218:221], v[22:25]
	v_mfma_f32_16x16x32_f16 v[18:21], v[234:237], v[218:221], v[18:21]
	v_mfma_f32_16x16x32_f16 v[70:73], v[230:233], v[198:201], v[70:73]
	v_mfma_f32_16x16x32_f16 v[66:69], v[238:241], v[198:201], v[66:69]
	v_mfma_f32_16x16x32_f16 v[54:57], v[230:233], v[206:209], v[54:57]
	v_mfma_f32_16x16x32_f16 v[50:53], v[238:241], v[206:209], v[50:53]
	v_mfma_f32_16x16x32_f16 v[38:41], v[230:233], v[214:217], v[38:41]
	v_mfma_f32_16x16x32_f16 v[34:37], v[238:241], v[214:217], v[34:37]
	v_mfma_f32_16x16x32_f16 v[22:25], v[230:233], v[222:225], v[22:25]
	v_mfma_f32_16x16x32_f16 v[18:21], v[238:241], v[222:225], v[18:21]
	s_setprio 0
	s_barrier
	s_add_i32 s81, s55, s45
	v_lshl_add_u64 v[170:171], v[170:171], 0, s[26:27]
	s_mov_b32 m0, s81
	global_load_lds_dwordx4 v[170:171], off
	v_lshl_add_u64 v[170:171], v[242:243], 0, s[26:27]
	s_add_i32 m0, s81, 0x2000
	s_nop 0
	global_load_lds_dwordx4 v[170:171], off
	s_add_i32 s82, s56, s45
	v_lshl_add_u64 v[248:249], v[244:245], 0, s[26:27]
	s_mov_b32 m0, s82
	s_nop 0
	global_load_lds_dwordx4 v[248:249], off
	v_lshl_add_u64 v[248:249], v[246:247], 0, s[26:27]
	s_add_i32 m0, s82, 0x2000
	s_nop 0
	global_load_lds_dwordx4 v[248:249], off
	s_add_i32 s34, s64, s70
	s_ashr_i32 s35, s34, 31
	s_waitcnt vmcnt(4)
	s_lshl_b64 s[34:35], s[34:35], 1
	v_pk_add_f16 v6, v6, v14
	v_pk_add_f16 v7, v7, v15
	v_pk_add_f16 v8, v8, v16
	v_pk_add_f16 v9, v9, v17
	s_add_u32 s34, s8, s34
	v_pk_max_f16 v9, v9, 0
	v_pk_max_f16 v8, v8, 0
	v_pk_max_f16 v7, v7, 0
	v_pk_max_f16 v6, v6, 0
	v_pk_add_f16 v10, v10, v14
	v_pk_add_f16 v11, v11, v15
	v_pk_add_f16 v12, v12, v16
	v_pk_add_f16 v13, v13, v17
	s_addc_u32 s35, s9, s35
	s_add_i32 s64, s67, s70
	v_pk_max_f16 v13, v13, 0
	v_pk_max_f16 v12, v12, 0
	v_pk_max_f16 v11, v11, 0
	v_pk_max_f16 v10, v10, 0
	ds_write_b128 v186, v[6:9] offset:32768
	ds_write_b128 v186, v[10:13] offset:40960
	s_ashr_i32 s65, s64, 31
	s_lshl_b64 s[64:65], s[64:65], 1
	s_nop 4
	global_load_dwordx4 v[14:17], v184, s[34:35]
	s_add_u32 s64, s10, s64
	global_load_dwordx4 v[6:9], v185, s[34:35]
	s_addc_u32 s65, s11, s65
	global_load_dwordx4 v[10:13], v183, s[64:65]
	s_waitcnt lgkmcnt(2)
	s_addk_i32 s62, 0x80
	s_add_u32 s59, s59, 0x100
	s_addc_u32 s60, s60, 0
	s_cmp_ge_i32 s61, s49
	s_barrier
	s_cbranch_scc0 .LBB8_12
	s_branch .LBB8_20

.LBB8_37:
	ds_read_b128 v[144:147], v173
	ds_read_b128 v[148:151], v173 offset:1024
	ds_read_b128 v[152:155], v173 offset:2048
	ds_read_b128 v[156:159], v173 offset:3072
	ds_read_b128 v[212:215], v177
	ds_read_b128 v[216:219], v177 offset:1024
	ds_read_b128 v[220:223], v177 offset:2048
	ds_read_b128 v[224:227], v177 offset:3072
	s_cmp_eq_u32 s49, s61
	s_cselect_b64 s[24:25], -1, 0
	s_and_b64 s[24:25], s[24:25], exec
	s_cselect_b32 s35, s23, s60
	s_cselect_b32 s34, s22, s59
	s_cselect_b32 s30, 0, s61
	s_cselect_b32 s31, s56, s57
	s_lshl_b32 s24, s30, 6
	s_lshl_b32 s62, s31, 14
	s_and_b32 s68, s24, 0x180
	s_or_b32 s24, s68, s62
	s_ashr_i32 s25, s24, 31
	s_lshl_b64 s[26:27], s[24:25], 1
	s_add_u32 s28, s8, s26
	s_addc_u32 s29, s9, s27
	s_lshl_b32 s25, s31, 6
	s_lshr_b32 s26, s30, 3
	ds_read_b128 v[180:183], v174
	ds_read_b128 v[184:187], v174 offset:1024
	ds_read_b128 v[188:191], v174 offset:2048
	ds_read_b128 v[192:195], v174 offset:3072
	ds_read_b128 v[196:199], v174 offset:4096
	ds_read_b128 v[200:203], v174 offset:5120
	ds_read_b128 v[204:207], v174 offset:6144
	ds_read_b128 v[208:211], v174 offset:7168
	s_waitcnt vmcnt(0)
	s_add_i32 s25, s25, s26
	v_pk_add_f16 v8, v8, v12
	v_pk_add_f16 v9, v9, v13
	v_pk_add_f16 v10, v10, v14
	v_pk_add_f16 v11, v11, v15
	s_lshl_b32 s63, s25, 9
	v_pk_max_f16 v11, v11, 0
	v_pk_max_f16 v10, v10, 0
	v_pk_max_f16 v9, v9, 0
	v_pk_max_f16 v8, v8, 0
	v_pk_add_f16 v0, v0, v4
	v_pk_add_f16 v1, v1, v5
	v_pk_add_f16 v2, v2, v6
	v_pk_add_f16 v3, v3, v7
	s_or_b32 s26, s63, s68
	v_pk_max_f16 v3, v3, 0
	v_pk_max_f16 v2, v2, 0
	v_pk_max_f16 v1, v1, 0
	v_pk_max_f16 v0, v0, 0
	ds_write_b128 v175, v[8:11] offset:49152
	ds_write_b128 v175, v[0:3] offset:57344
	s_ashr_i32 s27, s26, 31
	s_lshl_b64 s[30:31], s[26:27], 1
	s_nop 4
	global_load_dwordx4 v[0:3], v168, s[28:29]
	s_add_u32 s30, s10, s30
	global_load_dwordx4 v[4:7], v170, s[28:29]
	s_addc_u32 s31, s11, s31
	global_load_dwordx4 v[8:11], v169, s[30:31]
	global_load_dwordx4 v[12:15], v171, s[30:31]
	s_waitcnt lgkmcnt(2)
	s_barrier
	s_waitcnt lgkmcnt(0)
	s_setprio 1
	s_waitcnt lgkmcnt(0)
	v_mfma_f32_16x16x32_f16 v[136:139], v[144:147], v[180:183], v[136:139]
	v_mfma_f32_16x16x32_f16 v[140:143], v[152:155], v[180:183], v[140:143]
	v_mfma_f32_16x16x32_f16 v[124:127], v[144:147], v[188:191], v[124:127]
	v_mfma_f32_16x16x32_f16 v[120:123], v[152:155], v[188:191], v[120:123]
	v_mfma_f32_16x16x32_f16 v[108:111], v[144:147], v[196:199], v[108:111]
	v_mfma_f32_16x16x32_f16 v[104:107], v[152:155], v[196:199], v[104:107]
	v_mfma_f32_16x16x32_f16 v[92:95], v[144:147], v[204:207], v[92:95]
	v_mfma_f32_16x16x32_f16 v[88:91], v[152:155], v[204:207], v[88:91]
	v_mfma_f32_16x16x32_f16 v[136:139], v[148:151], v[184:187], v[136:139]
	v_mfma_f32_16x16x32_f16 v[140:143], v[156:159], v[184:187], v[140:143]
	v_mfma_f32_16x16x32_f16 v[124:127], v[148:151], v[192:195], v[124:127]
	v_mfma_f32_16x16x32_f16 v[120:123], v[156:159], v[192:195], v[120:123]
	v_mfma_f32_16x16x32_f16 v[108:111], v[148:151], v[200:203], v[108:111]
	v_mfma_f32_16x16x32_f16 v[104:107], v[156:159], v[200:203], v[104:107]
	v_mfma_f32_16x16x32_f16 v[92:95], v[148:151], v[208:211], v[92:95]
	v_mfma_f32_16x16x32_f16 v[88:91], v[156:159], v[208:211], v[88:91]
	s_setprio 0
	s_waitcnt lgkmcnt(0)
	s_setprio 1
	s_waitcnt lgkmcnt(0)
	v_mfma_f32_16x16x32_f16 v[132:135], v[212:215], v[180:183], v[132:135]
	v_mfma_f32_16x16x32_f16 v[128:131], v[220:223], v[180:183], v[128:131]
	v_mfma_f32_16x16x32_f16 v[116:119], v[212:215], v[188:191], v[116:119]
	v_mfma_f32_16x16x32_f16 v[112:115], v[220:223], v[188:191], v[112:115]
	v_mfma_f32_16x16x32_f16 v[100:103], v[212:215], v[196:199], v[100:103]
	v_mfma_f32_16x16x32_f16 v[96:99], v[220:223], v[196:199], v[96:99]
	v_mfma_f32_16x16x32_f16 v[84:87], v[212:215], v[204:207], v[84:87]
	v_mfma_f32_16x16x32_f16 v[80:83], v[220:223], v[204:207], v[80:83]
	ds_read_b128 v[180:183], v174 offset:16384
	ds_read_b128 v[188:191], v174 offset:18432
	ds_read_b128 v[196:199], v174 offset:20480
	ds_read_b128 v[204:207], v174 offset:22528
	v_mfma_f32_16x16x32_f16 v[132:135], v[216:219], v[184:187], v[132:135]
	v_mfma_f32_16x16x32_f16 v[128:131], v[224:227], v[184:187], v[128:131]
	v_mfma_f32_16x16x32_f16 v[116:119], v[216:219], v[192:195], v[116:119]
	v_mfma_f32_16x16x32_f16 v[112:115], v[224:227], v[192:195], v[112:115]
	v_mfma_f32_16x16x32_f16 v[100:103], v[216:219], v[200:203], v[100:103]
	v_mfma_f32_16x16x32_f16 v[96:99], v[224:227], v[200:203], v[96:99]
	v_mfma_f32_16x16x32_f16 v[84:87], v[216:219], v[208:211], v[84:87]
	v_mfma_f32_16x16x32_f16 v[80:83], v[224:227], v[208:211], v[80:83]
	ds_read_b128 v[184:187], v174 offset:17408
	ds_read_b128 v[192:195], v174 offset:19456
	ds_read_b128 v[200:203], v174 offset:21504
	ds_read_b128 v[208:211], v174 offset:23552
	s_waitcnt lgkmcnt(4)
	s_setprio 1
	s_waitcnt lgkmcnt(4)
	v_mfma_f32_16x16x32_f16 v[76:79], v[144:147], v[180:183], v[76:79]
	v_mfma_f32_16x16x32_f16 v[72:75], v[152:155], v[180:183], v[72:75]
	v_mfma_f32_16x16x32_f16 v[60:63], v[144:147], v[188:191], v[60:63]
	v_mfma_f32_16x16x32_f16 v[56:59], v[152:155], v[188:191], v[56:59]
	v_mfma_f32_16x16x32_f16 v[44:47], v[144:147], v[196:199], v[44:47]
	v_mfma_f32_16x16x32_f16 v[40:43], v[152:155], v[196:199], v[40:43]
	v_mfma_f32_16x16x32_f16 v[28:31], v[144:147], v[204:207], v[28:31]
	v_mfma_f32_16x16x32_f16 v[24:27], v[152:155], v[204:207], v[24:27]
	s_waitcnt lgkmcnt(0)
	v_mfma_f32_16x16x32_f16 v[76:79], v[148:151], v[184:187], v[76:79]
	v_mfma_f32_16x16x32_f16 v[72:75], v[156:159], v[184:187], v[72:75]
	v_mfma_f32_16x16x32_f16 v[60:63], v[148:151], v[192:195], v[60:63]
	v_mfma_f32_16x16x32_f16 v[56:59], v[156:159], v[192:195], v[56:59]
	v_mfma_f32_16x16x32_f16 v[44:47], v[148:151], v[200:203], v[44:47]
	v_mfma_f32_16x16x32_f16 v[40:43], v[156:159], v[200:203], v[40:43]
	v_mfma_f32_16x16x32_f16 v[28:31], v[148:151], v[208:211], v[28:31]
	v_mfma_f32_16x16x32_f16 v[24:27], v[156:159], v[208:211], v[24:27]
	s_setprio 0
	s_setprio 1
	v_mfma_f32_16x16x32_f16 v[68:71], v[212:215], v[180:183], v[68:71]
	v_mfma_f32_16x16x32_f16 v[64:67], v[220:223], v[180:183], v[64:67]
	v_mfma_f32_16x16x32_f16 v[52:55], v[212:215], v[188:191], v[52:55]
	v_mfma_f32_16x16x32_f16 v[48:51], v[220:223], v[188:191], v[48:51]
	v_mfma_f32_16x16x32_f16 v[36:39], v[212:215], v[196:199], v[36:39]
	v_mfma_f32_16x16x32_f16 v[32:35], v[220:223], v[196:199], v[32:35]
	v_mfma_f32_16x16x32_f16 v[20:23], v[212:215], v[204:207], v[20:23]
	v_mfma_f32_16x16x32_f16 v[16:19], v[220:223], v[204:207], v[16:19]
	v_mfma_f32_16x16x32_f16 v[68:71], v[216:219], v[184:187], v[68:71]
	v_mfma_f32_16x16x32_f16 v[64:67], v[224:227], v[184:187], v[64:67]
	v_mfma_f32_16x16x32_f16 v[52:55], v[216:219], v[192:195], v[52:55]
	v_mfma_f32_16x16x32_f16 v[48:51], v[224:227], v[192:195], v[48:51]
	v_mfma_f32_16x16x32_f16 v[36:39], v[216:219], v[200:203], v[36:39]
	v_mfma_f32_16x16x32_f16 v[32:35], v[224:227], v[200:203], v[32:35]
	v_mfma_f32_16x16x32_f16 v[20:23], v[216:219], v[208:211], v[20:23]
	v_mfma_f32_16x16x32_f16 v[16:19], v[224:227], v[208:211], v[16:19]
	s_setprio 0
	s_or_b32 s64, s62, 0x2000
	s_or_b32 s28, s68, s64
	s_ashr_i32 s29, s28, 31
	s_barrier
	s_add_i32 s81, s51, s44
	v_lshl_add_u64 v[166:167], s[34:35], 0, v[160:161]
	s_mov_b32 m0, s81
	global_load_lds_dwordx4 v[166:167], off
	v_lshl_add_u64 v[228:229], s[34:35], 0, v[162:163]
	s_add_i32 m0, s81, 0x2000
	s_nop 0
	global_load_lds_dwordx4 v[228:229], off
	s_add_u32 s34, s34, s14
	s_addc_u32 s35, s35, s15
	s_add_i32 s82, s52, s44
	v_lshl_add_u64 v[230:231], s[34:35], 0, v[160:161]
	s_mov_b32 m0, s82
	v_lshl_add_u64 v[232:233], s[34:35], 0, v[162:163]
	global_load_lds_dwordx4 v[230:231], off
	s_add_i32 m0, s82, 0x2000
	s_nop 0
	global_load_lds_dwordx4 v[232:233], off
	s_lshl_b64 s[30:31], s[28:29], 1
	s_waitcnt vmcnt(4)
	s_add_u32 s66, s8, s30
	v_pk_add_f16 v0, v0, v8
	v_pk_add_f16 v1, v1, v9
	v_pk_add_f16 v2, v2, v10
	v_pk_add_f16 v3, v3, v11
	s_addc_u32 s67, s9, s31
	s_add_i32 s65, s63, 0x4000
	v_pk_max_f16 v3, v3, 0
	v_pk_max_f16 v2, v2, 0
	v_pk_max_f16 v1, v1, 0
	v_pk_max_f16 v0, v0, 0
	v_pk_add_f16 v4, v4, v12
	v_pk_add_f16 v5, v5, v13
	v_pk_add_f16 v6, v6, v14
	v_pk_add_f16 v7, v7, v15
	s_or_b32 s30, s65, s68
	v_pk_max_f16 v7, v7, 0
	v_pk_max_f16 v6, v6, 0
	v_pk_max_f16 v5, v5, 0
	v_pk_max_f16 v4, v4, 0
	ds_write_b128 v175, v[0:3]
	ds_write_b128 v175, v[4:7] offset:8192
	s_ashr_i32 s31, s30, 31
	s_lshl_b64 s[68:69], s[30:31], 1
	s_nop 4
	global_load_dwordx4 v[0:3], v168, s[66:67]
	s_add_u32 s68, s10, s68
	global_load_dwordx4 v[4:7], v170, s[66:67]
	s_addc_u32 s69, s11, s69
	global_load_dwordx4 v[8:11], v169, s[68:69]
	global_load_dwordx4 v[12:15], v171, s[68:69]
	s_waitcnt lgkmcnt(2)
	s_barrier
	ds_read_b128 v[144:147], v178
	ds_read_b128 v[148:151], v178 offset:1024
	ds_read_b128 v[152:155], v178 offset:2048
	ds_read_b128 v[156:159], v178 offset:3072
	ds_read_b128 v[212:215], v179
	ds_read_b128 v[216:219], v179 offset:1024
	ds_read_b128 v[220:223], v179 offset:2048
	ds_read_b128 v[224:227], v179 offset:3072
	s_ashr_i32 s25, s62, 31
	s_lshl_b64 s[24:25], s[24:25], 1
	s_add_u32 s24, s8, s24
	s_addc_u32 s25, s9, s25
	ds_read_b128 v[180:183], v174 offset:32768
	ds_read_b128 v[184:187], v174 offset:33792
	ds_read_b128 v[188:191], v174 offset:34816
	ds_read_b128 v[192:195], v174 offset:35840
	ds_read_b128 v[196:199], v174 offset:36864
	ds_read_b128 v[200:203], v174 offset:37888
	ds_read_b128 v[204:207], v174 offset:38912
	ds_read_b128 v[208:211], v174 offset:39936
	s_waitcnt vmcnt(0)
	s_add_u32 s24, s24, 0x80
	v_pk_add_f16 v0, v0, v8
	v_pk_add_f16 v1, v1, v9
	v_pk_add_f16 v2, v2, v10
	v_pk_add_f16 v3, v3, v11
	s_addc_u32 s25, s25, 0
	s_ashr_i32 s27, s63, 31
	v_pk_max_f16 v3, v3, 0
	v_pk_max_f16 v2, v2, 0
	v_pk_max_f16 v1, v1, 0
	v_pk_max_f16 v0, v0, 0
	v_pk_add_f16 v4, v4, v12
	v_pk_add_f16 v5, v5, v13
	v_pk_add_f16 v6, v6, v14
	v_pk_add_f16 v7, v7, v15
	s_lshl_b64 s[26:27], s[26:27], 1
	v_pk_max_f16 v7, v7, 0
	v_pk_max_f16 v6, v6, 0
	v_pk_max_f16 v5, v5, 0
	v_pk_max_f16 v4, v4, 0
	ds_write_b128 v175, v[0:3] offset:16384
	ds_write_b128 v175, v[4:7] offset:24576
	s_add_u32 s26, s10, s26
	s_addc_u32 s27, s11, s27
	s_nop 4
	global_load_dwordx4 v[0:3], v168, s[24:25]
	s_add_u32 s26, s26, 0x80
	global_load_dwordx4 v[4:7], v170, s[24:25]
	s_addc_u32 s27, s27, 0
	global_load_dwordx4 v[8:11], v169, s[26:27]
	global_load_dwordx4 v[12:15], v171, s[26:27]
	s_waitcnt lgkmcnt(2)
	s_barrier
	s_waitcnt lgkmcnt(0)
	s_setprio 1
	s_waitcnt lgkmcnt(0)
	v_mfma_f32_16x16x32_f16 v[136:139], v[144:147], v[180:183], v[136:139]
	v_mfma_f32_16x16x32_f16 v[140:143], v[152:155], v[180:183], v[140:143]
	v_mfma_f32_16x16x32_f16 v[124:127], v[144:147], v[188:191], v[124:127]
	v_mfma_f32_16x16x32_f16 v[120:123], v[152:155], v[188:191], v[120:123]
	v_mfma_f32_16x16x32_f16 v[108:111], v[144:147], v[196:199], v[108:111]
	v_mfma_f32_16x16x32_f16 v[104:107], v[152:155], v[196:199], v[104:107]
	v_mfma_f32_16x16x32_f16 v[92:95], v[144:147], v[204:207], v[92:95]
	v_mfma_f32_16x16x32_f16 v[88:91], v[152:155], v[204:207], v[88:91]
	v_mfma_f32_16x16x32_f16 v[136:139], v[148:151], v[184:187], v[136:139]
	v_mfma_f32_16x16x32_f16 v[140:143], v[156:159], v[184:187], v[140:143]
	v_mfma_f32_16x16x32_f16 v[124:127], v[148:151], v[192:195], v[124:127]
	v_mfma_f32_16x16x32_f16 v[120:123], v[156:159], v[192:195], v[120:123]
	v_mfma_f32_16x16x32_f16 v[108:111], v[148:151], v[200:203], v[108:111]
	v_mfma_f32_16x16x32_f16 v[104:107], v[156:159], v[200:203], v[104:107]
	v_mfma_f32_16x16x32_f16 v[92:95], v[148:151], v[208:211], v[92:95]
	v_mfma_f32_16x16x32_f16 v[88:91], v[156:159], v[208:211], v[88:91]
	s_setprio 0
	s_waitcnt lgkmcnt(0)
	s_setprio 1
	s_waitcnt lgkmcnt(0)
	v_mfma_f32_16x16x32_f16 v[132:135], v[212:215], v[180:183], v[132:135]
	v_mfma_f32_16x16x32_f16 v[128:131], v[220:223], v[180:183], v[128:131]
	v_mfma_f32_16x16x32_f16 v[116:119], v[212:215], v[188:191], v[116:119]
	v_mfma_f32_16x16x32_f16 v[112:115], v[220:223], v[188:191], v[112:115]
	v_mfma_f32_16x16x32_f16 v[100:103], v[212:215], v[196:199], v[100:103]
	v_mfma_f32_16x16x32_f16 v[96:99], v[220:223], v[196:199], v[96:99]
	v_mfma_f32_16x16x32_f16 v[84:87], v[212:215], v[204:207], v[84:87]
	v_mfma_f32_16x16x32_f16 v[80:83], v[220:223], v[204:207], v[80:83]
	ds_read_b128 v[180:183], v174 offset:49152
	ds_read_b128 v[188:191], v174 offset:51200
	ds_read_b128 v[196:199], v174 offset:53248
	ds_read_b128 v[204:207], v174 offset:55296
	v_mfma_f32_16x16x32_f16 v[132:135], v[216:219], v[184:187], v[132:135]
	v_mfma_f32_16x16x32_f16 v[128:131], v[224:227], v[184:187], v[128:131]
	v_mfma_f32_16x16x32_f16 v[116:119], v[216:219], v[192:195], v[116:119]
	v_mfma_f32_16x16x32_f16 v[112:115], v[224:227], v[192:195], v[112:115]
	v_mfma_f32_16x16x32_f16 v[100:103], v[216:219], v[200:203], v[100:103]
	v_mfma_f32_16x16x32_f16 v[96:99], v[224:227], v[200:203], v[96:99]
	v_mfma_f32_16x16x32_f16 v[84:87], v[216:219], v[208:211], v[84:87]
	v_mfma_f32_16x16x32_f16 v[80:83], v[224:227], v[208:211], v[80:83]
	ds_read_b128 v[184:187], v174 offset:50176
	ds_read_b128 v[192:195], v174 offset:52224
	ds_read_b128 v[200:203], v174 offset:54272
	ds_read_b128 v[208:211], v174 offset:56320
	s_waitcnt lgkmcnt(4)
	s_setprio 1
	s_waitcnt lgkmcnt(4)
	v_mfma_f32_16x16x32_f16 v[76:79], v[144:147], v[180:183], v[76:79]
	v_mfma_f32_16x16x32_f16 v[72:75], v[152:155], v[180:183], v[72:75]
	v_mfma_f32_16x16x32_f16 v[60:63], v[144:147], v[188:191], v[60:63]
	v_mfma_f32_16x16x32_f16 v[56:59], v[152:155], v[188:191], v[56:59]
	v_mfma_f32_16x16x32_f16 v[44:47], v[144:147], v[196:199], v[44:47]
	v_mfma_f32_16x16x32_f16 v[40:43], v[152:155], v[196:199], v[40:43]
	v_mfma_f32_16x16x32_f16 v[28:31], v[144:147], v[204:207], v[28:31]
	v_mfma_f32_16x16x32_f16 v[24:27], v[152:155], v[204:207], v[24:27]
	s_waitcnt lgkmcnt(0)
	v_mfma_f32_16x16x32_f16 v[76:79], v[148:151], v[184:187], v[76:79]
	v_mfma_f32_16x16x32_f16 v[72:75], v[156:159], v[184:187], v[72:75]
	v_mfma_f32_16x16x32_f16 v[60:63], v[148:151], v[192:195], v[60:63]
	v_mfma_f32_16x16x32_f16 v[56:59], v[156:159], v[192:195], v[56:59]
	v_mfma_f32_16x16x32_f16 v[44:47], v[148:151], v[200:203], v[44:47]
	v_mfma_f32_16x16x32_f16 v[40:43], v[156:159], v[200:203], v[40:43]
	v_mfma_f32_16x16x32_f16 v[28:31], v[148:151], v[208:211], v[28:31]
	v_mfma_f32_16x16x32_f16 v[24:27], v[156:159], v[208:211], v[24:27]
	s_setprio 0
	s_setprio 1
	v_mfma_f32_16x16x32_f16 v[68:71], v[212:215], v[180:183], v[68:71]
	v_mfma_f32_16x16x32_f16 v[64:67], v[220:223], v[180:183], v[64:67]
	v_mfma_f32_16x16x32_f16 v[52:55], v[212:215], v[188:191], v[52:55]
	v_mfma_f32_16x16x32_f16 v[48:51], v[220:223], v[188:191], v[48:51]
	v_mfma_f32_16x16x32_f16 v[36:39], v[212:215], v[196:199], v[36:39]
	v_mfma_f32_16x16x32_f16 v[32:35], v[220:223], v[196:199], v[32:35]
	v_mfma_f32_16x16x32_f16 v[20:23], v[212:215], v[204:207], v[20:23]
	v_mfma_f32_16x16x32_f16 v[16:19], v[220:223], v[204:207], v[16:19]
	v_mfma_f32_16x16x32_f16 v[68:71], v[216:219], v[184:187], v[68:71]
	v_mfma_f32_16x16x32_f16 v[64:67], v[224:227], v[184:187], v[64:67]
	v_mfma_f32_16x16x32_f16 v[52:55], v[216:219], v[192:195], v[52:55]
	v_mfma_f32_16x16x32_f16 v[48:51], v[224:227], v[192:195], v[48:51]
	v_mfma_f32_16x16x32_f16 v[36:39], v[216:219], v[200:203], v[36:39]
	v_mfma_f32_16x16x32_f16 v[32:35], v[224:227], v[200:203], v[32:35]
	v_mfma_f32_16x16x32_f16 v[20:23], v[216:219], v[208:211], v[20:23]
	v_mfma_f32_16x16x32_f16 v[16:19], v[224:227], v[208:211], v[16:19]
	s_setprio 0
	s_ashr_i32 s29, s64, 31
	s_lshl_b64 s[24:25], s[28:29], 1
	s_add_u32 s24, s8, s24
	s_barrier
	s_add_i32 s81, s53, s44
	v_lshl_add_u64 v[166:167], v[166:167], 0, s[20:21]
	s_mov_b32 m0, s81
	global_load_lds_dwordx4 v[166:167], off
	v_lshl_add_u64 v[166:167], v[228:229], 0, s[20:21]
	s_add_i32 m0, s81, 0x2000
	s_nop 0
	global_load_lds_dwordx4 v[166:167], off
	s_add_i32 s82, s54, s44
	v_lshl_add_u64 v[248:249], v[230:231], 0, s[20:21]
	s_mov_b32 m0, s82
	s_nop 0
	global_load_lds_dwordx4 v[248:249], off
	v_lshl_add_u64 v[248:249], v[232:233], 0, s[20:21]
	s_add_i32 m0, s82, 0x2000
	s_nop 0
	global_load_lds_dwordx4 v[248:249], off
	s_addc_u32 s25, s9, s25
	s_waitcnt vmcnt(4)
	s_add_u32 s24, s24, 0x80
	v_pk_add_f16 v0, v0, v8
	v_pk_add_f16 v1, v1, v9
	v_pk_add_f16 v2, v2, v10
	v_pk_add_f16 v3, v3, v11
	s_addc_u32 s25, s25, 0
	s_ashr_i32 s31, s65, 31
	v_pk_max_f16 v3, v3, 0
	v_pk_max_f16 v2, v2, 0
	v_pk_max_f16 v1, v1, 0
	v_pk_max_f16 v0, v0, 0
	v_pk_add_f16 v4, v4, v12
	v_pk_add_f16 v5, v5, v13
	v_pk_add_f16 v6, v6, v14
	v_pk_add_f16 v7, v7, v15
	s_lshl_b64 s[26:27], s[30:31], 1
	v_pk_max_f16 v7, v7, 0
	v_pk_max_f16 v6, v6, 0
	v_pk_max_f16 v5, v5, 0
	v_pk_max_f16 v4, v4, 0
	ds_write_b128 v175, v[0:3] offset:32768
	ds_write_b128 v175, v[4:7] offset:40960
	s_add_u32 s26, s10, s26
	s_addc_u32 s27, s11, s27
	s_nop 4
	global_load_dwordx4 v[8:11], v168, s[24:25]
	s_add_u32 s26, s26, 0x80
	global_load_dwordx4 v[0:3], v170, s[24:25]
	s_addc_u32 s27, s27, 0
	global_load_dwordx4 v[12:15], v169, s[26:27]
	global_load_dwordx4 v[4:7], v171, s[26:27]
	s_waitcnt lgkmcnt(2)
	s_add_i32 s24, s61, 2
	s_add_u32 s59, s59, 0x100
	s_addc_u32 s60, s60, 0
	s_cmp_ge_i32 s61, s49
	s_mov_b32 s61, s24
	s_barrier
	s_cbranch_scc0 .LBB8_37
	s_branch .LBB8_45
